# v64 + grid-barrier spin loops poll without the s_sleep back-off
# speedup vs baseline: 1.0029x; 1.0029x over previous
.LBB0_103:
	global_load_dword v16, v17, s[4:5] sc1
	global_load_dword v1, v17, s[6:7] sc1
	global_load_dword v2, v17, s[8:9] sc1
	global_load_dword v3, v17, s[10:11] sc1
	global_load_dword v4, v17, s[12:13] sc1
	global_load_dword v5, v17, s[14:15] sc1
	global_load_dword v6, v17, s[16:17] sc1
	global_load_dword v7, v17, s[18:19] sc1
	global_load_dword v8, v17, s[20:21] sc1
	global_load_dword v9, v17, s[22:23] sc1
	global_load_dword v10, v17, s[24:25] sc1
	global_load_dword v11, v17, s[26:27] sc1
	global_load_dword v12, v17, s[28:29] sc1
	global_load_dword v13, v17, s[30:31] sc1
	global_load_dword v14, v17, s[34:35] sc1
	global_load_dword v15, v17, s[38:39] sc1
	s_mov_b64 s[40:41], -1
	s_mov_b64 s[42:43], -1
	s_waitcnt vmcnt(14)
	v_add_u32_e32 v18, v1, v16
	s_waitcnt vmcnt(13)
	v_add_u32_e32 v18, v18, v2
	s_waitcnt vmcnt(12)
	v_add_u32_e32 v18, v18, v3
	s_waitcnt vmcnt(11)
	v_add_u32_e32 v18, v18, v4
	s_waitcnt vmcnt(10)
	v_add_u32_e32 v18, v18, v5
	s_waitcnt vmcnt(9)
	v_add_u32_e32 v18, v18, v6
	s_waitcnt vmcnt(8)
	v_add_u32_e32 v18, v18, v7
	s_waitcnt vmcnt(7)
	v_add_u32_e32 v18, v18, v8
	s_waitcnt vmcnt(6)
	v_add_u32_e32 v18, v18, v9
	s_waitcnt vmcnt(5)
	v_add_u32_e32 v18, v18, v10
	s_waitcnt vmcnt(4)
	v_add_u32_e32 v18, v18, v11
	s_waitcnt vmcnt(3)
	v_add_u32_e32 v18, v18, v12
	s_waitcnt vmcnt(2)
	v_add_u32_e32 v18, v18, v13
	s_waitcnt vmcnt(1)
	v_add_u32_e32 v18, v18, v14
	s_waitcnt vmcnt(0)
	v_add_u32_e32 v18, v18, v15
	v_cmp_eq_u32_e32 vcc, s33, v18
	s_cbranch_vccnz .LBB0_102
	s_and_b32 s40, s46, 0xff
	s_cmp_eq_u32 s40, 0
	s_mov_b64 s[40:41], -1
	s_mov_b64 s[44:45], -1
	s_sleep 0
	s_cbranch_scc0 .LBB0_107
	global_load_dword v18, v17, s[2:3] sc1
	s_waitcnt vmcnt(0)
	v_cmp_eq_u32_e32 vcc, 0, v18
	s_cbranch_vccnz .LBB0_109
	s_mov_b64 s[44:45], 0

.LBB0_120:
	s_and_b32 s18, s22, 0xff
	s_mov_b64 s[16:17], -1
	s_cmp_lg_u32 s18, 0
	s_mov_b64 s[20:21], -1
	s_sleep 0
	s_cbranch_scc1 .LBB0_123
	global_load_dword v3, v1, s[8:9] sc1
	s_waitcnt vmcnt(0)
	v_cmp_eq_u32_e32 vcc, 0, v3
	s_cbranch_vccnz .LBB0_125
	s_mov_b64 s[20:21], 0
	s_mov_b64 s[18:19], -1

.LBB0_137:
	s_and_b32 s16, s22, 0xff
	s_cmp_lg_u32 s16, 0
	s_mov_b64 s[18:19], -1
	s_sleep 0
	s_cbranch_scc1 .LBB0_140
	global_load_dword v2, v1, s[8:9] sc1
	s_waitcnt vmcnt(0)
	v_cmp_eq_u32_e32 vcc, 0, v2
	s_cbranch_vccnz .LBB0_142
	s_mov_b64 s[18:19], 0
	s_mov_b64 s[16:17], -1

.LBB0_571:
	global_load_dword v16, v17, s[4:5] sc1
	global_load_dword v1, v17, s[6:7] sc1
	global_load_dword v2, v17, s[8:9] sc1
	global_load_dword v3, v17, s[10:11] sc1
	global_load_dword v4, v17, s[12:13] sc1
	global_load_dword v5, v17, s[14:15] sc1
	global_load_dword v6, v17, s[16:17] sc1
	global_load_dword v7, v17, s[18:19] sc1
	global_load_dword v8, v17, s[20:21] sc1
	global_load_dword v9, v17, s[22:23] sc1
	global_load_dword v10, v17, s[24:25] sc1
	global_load_dword v11, v17, s[26:27] sc1
	global_load_dword v12, v17, s[28:29] sc1
	global_load_dword v13, v17, s[30:31] sc1
	global_load_dword v14, v17, s[34:35] sc1
	global_load_dword v15, v17, s[38:39] sc1
	s_mov_b64 s[40:41], -1
	s_mov_b64 s[42:43], -1
	s_waitcnt vmcnt(14)
	v_add_u32_e32 v18, v1, v16
	s_waitcnt vmcnt(13)
	v_add_u32_e32 v18, v18, v2
	s_waitcnt vmcnt(12)
	v_add_u32_e32 v18, v18, v3
	s_waitcnt vmcnt(11)
	v_add_u32_e32 v18, v18, v4
	s_waitcnt vmcnt(10)
	v_add_u32_e32 v18, v18, v5
	s_waitcnt vmcnt(9)
	v_add_u32_e32 v18, v18, v6
	s_waitcnt vmcnt(8)
	v_add_u32_e32 v18, v18, v7
	s_waitcnt vmcnt(7)
	v_add_u32_e32 v18, v18, v8
	s_waitcnt vmcnt(6)
	v_add_u32_e32 v18, v18, v9
	s_waitcnt vmcnt(5)
	v_add_u32_e32 v18, v18, v10
	s_waitcnt vmcnt(4)
	v_add_u32_e32 v18, v18, v11
	s_waitcnt vmcnt(3)
	v_add_u32_e32 v18, v18, v12
	s_waitcnt vmcnt(2)
	v_add_u32_e32 v18, v18, v13
	s_waitcnt vmcnt(1)
	v_add_u32_e32 v18, v18, v14
	s_waitcnt vmcnt(0)
	v_add_u32_e32 v18, v18, v15
	v_cmp_eq_u32_e32 vcc, s33, v18
	s_cbranch_vccnz .LBB0_570
	s_and_b32 s40, s47, 0xff
	s_cmp_eq_u32 s40, 0
	s_mov_b64 s[40:41], -1
	s_mov_b64 s[44:45], -1
	s_sleep 0
	s_cbranch_scc0 .LBB0_575
	global_load_dword v18, v17, s[2:3] sc1
	s_waitcnt vmcnt(0)
	v_cmp_eq_u32_e32 vcc, 0, v18
	s_cbranch_vccnz .LBB0_577
	s_mov_b64 s[44:45], 0

.LBB0_856:
	global_load_dword v16, v17, s[4:5] sc1
	global_load_dword v1, v17, s[6:7] sc1
	global_load_dword v2, v17, s[8:9] sc1
	global_load_dword v3, v17, s[10:11] sc1
	global_load_dword v4, v17, s[12:13] sc1
	global_load_dword v5, v17, s[14:15] sc1
	global_load_dword v6, v17, s[16:17] sc1
	global_load_dword v7, v17, s[18:19] sc1
	global_load_dword v8, v17, s[20:21] sc1
	global_load_dword v9, v17, s[22:23] sc1
	global_load_dword v10, v17, s[24:25] sc1
	global_load_dword v11, v17, s[26:27] sc1
	global_load_dword v12, v17, s[28:29] sc1
	global_load_dword v13, v17, s[30:31] sc1
	global_load_dword v14, v17, s[34:35] sc1
	global_load_dword v15, v17, s[36:37] sc1
	s_mov_b64 s[38:39], -1
	s_mov_b64 s[40:41], -1
	s_waitcnt vmcnt(14)
	v_add_u32_e32 v18, v1, v16
	s_waitcnt vmcnt(13)
	v_add_u32_e32 v18, v18, v2
	s_waitcnt vmcnt(12)
	v_add_u32_e32 v18, v18, v3
	s_waitcnt vmcnt(11)
	v_add_u32_e32 v18, v18, v4
	s_waitcnt vmcnt(10)
	v_add_u32_e32 v18, v18, v5
	s_waitcnt vmcnt(9)
	v_add_u32_e32 v18, v18, v6
	s_waitcnt vmcnt(8)
	v_add_u32_e32 v18, v18, v7
	s_waitcnt vmcnt(7)
	v_add_u32_e32 v18, v18, v8
	s_waitcnt vmcnt(6)
	v_add_u32_e32 v18, v18, v9
	s_waitcnt vmcnt(5)
	v_add_u32_e32 v18, v18, v10
	s_waitcnt vmcnt(4)
	v_add_u32_e32 v18, v18, v11
	s_waitcnt vmcnt(3)
	v_add_u32_e32 v18, v18, v12
	s_waitcnt vmcnt(2)
	v_add_u32_e32 v18, v18, v13
	s_waitcnt vmcnt(1)
	v_add_u32_e32 v18, v18, v14
	s_waitcnt vmcnt(0)
	v_add_u32_e32 v18, v18, v15
	v_cmp_eq_u32_e32 vcc, s33, v18
	s_cbranch_vccnz .LBB0_855
	s_and_b32 s38, s44, 0xff
	s_cmp_eq_u32 s38, 0
	s_mov_b64 s[38:39], -1
	s_mov_b64 s[42:43], -1
	s_sleep 0
	s_cbranch_scc0 .LBB0_860
	global_load_dword v18, v17, s[2:3] sc1
	s_waitcnt vmcnt(0)
	v_cmp_eq_u32_e32 vcc, 0, v18
	s_cbranch_vccnz .LBB0_862
	s_mov_b64 s[42:43], 0
